# k_mid and k_prep block order rotated so the small latency-chained blocks (colsum, folded params) are dispatched first
# speedup vs baseline: 1.0106x; 1.0011x over previous
_ZN2rb6k_prepEPKfS1_S1_S1_S1_S1_S1_S1_Phi:
	s_addk_i32 s2, 0x1200
	s_cmpk_lt_u32 s2, 0x1208
	s_cbranch_scc1 .Lprep_rot
	s_sub_i32 s2, s2, 0x1208
.Lprep_rot:
	s_load_dword s3, s[0:1], 0x48
	s_load_dwordx2 s[12:13], s[0:1], 0x40
	s_mov_b64 s[4:5], -1
	s_waitcnt lgkmcnt(0)
	s_add_i32 s2, s3, s2
	s_cmpk_gt_i32 s2, 0x1ff
	s_cbranch_scc1 .LBB0_3
	s_andn2_b64 vcc, exec, s[4:5]
	s_cbranch_vccz .LBB0_16

_ZN2rb5k_midEPhPKf:
	s_add_i32 s2, s2, 0x500
	s_cmpk_lt_u32 s2, 0x508
	s_cbranch_scc1 .Lmid_rot
	s_sub_i32 s2, s2, 0x508
.Lmid_rot:
	s_load_dwordx2 s[6:7], s[0:1], 0x0
	s_cmpk_gt_i32 s2, 0xff
	s_mov_b64 s[4:5], -1
	s_cbranch_scc1 .LBB1_3
	s_andn2_b64 vcc, exec, s[4:5]
	s_cbranch_vccz .LBB1_22
